# P5: norm_ffn gain slice staged in LDS at the top of the token block; h2 section reads it with ds_read_b128 instead of four global fetches queued behind the h2 stores
# speedup vs baseline: 1.0184x; 1.0021x over previous
.LBB0_1035:
	s_and_saveexec_b64 s[0:1], s[22:23]
	ds_write_b32 v253, v251
	s_or_b64 exec, exec, s[0:1]
	s_lshl_b32 s35, s38, 6
	v_or_b32_e32 v66, s35, v252
	v_ashrrev_i32_e32 v67, 31, v66
	v_lshlrev_b64 v[68:69], 11, v[66:67]
	v_lshl_add_u64 v[68:69], v[134:135], 0, v[68:69]
	v_mbcnt_lo_u32_b32 v130, -1, 0
	v_mbcnt_hi_u32_b32 v130, -1, v130
	v_and_b32_e32 v131, 7, v130
	v_lshrrev_b32_e32 v132, 1, v131
	v_and_b32_e32 v131, 1, v131
	v_lshlrev_b32_e32 v132, 7, v132
	v_lshl_or_b32 v132, v131, 4, v132
	v_mov_b32_e32 v133, 0
	v_lshl_add_u64 v[132:133], v[138:139], 0, v[132:133]
	global_load_dwordx4 v[130:133], v[132:133], off
	global_load_dwordx4 v[126:129], v[68:69], off nt
	global_load_dwordx4 v[122:125], v[68:69], off offset:64 nt
	global_load_dwordx4 v[118:121], v[68:69], off offset:128 nt
	global_load_dwordx4 v[114:117], v[68:69], off offset:192 nt
	v_or_b32_e32 v68, 16, v66
	v_or_b32_e32 v70, 32, v66
	v_or_b32_e32 v66, 48, v66
	v_ashrrev_i32_e32 v69, 31, v68
	v_ashrrev_i32_e32 v71, 31, v70
	v_ashrrev_i32_e32 v67, 31, v66
	v_lshlrev_b64 v[68:69], 11, v[68:69]
	v_lshlrev_b64 v[70:71], 11, v[70:71]
	v_lshlrev_b64 v[66:67], 11, v[66:67]
	v_lshl_add_u64 v[68:69], v[134:135], 0, v[68:69]
	v_lshl_add_u64 v[70:71], v[134:135], 0, v[70:71]
	v_lshl_add_u64 v[66:67], v[134:135], 0, v[66:67]
	global_load_dwordx4 v[110:113], v[68:69], off nt
	global_load_dwordx4 v[106:109], v[68:69], off offset:64 nt
	global_load_dwordx4 v[102:105], v[68:69], off offset:128 nt
	global_load_dwordx4 v[98:101], v[68:69], off offset:192 nt
	global_load_dwordx4 v[94:97], v[70:71], off nt
	global_load_dwordx4 v[90:93], v[70:71], off offset:64 nt
	global_load_dwordx4 v[86:89], v[70:71], off offset:128 nt
	global_load_dwordx4 v[82:85], v[70:71], off offset:192 nt
	global_load_dwordx4 v[78:81], v[66:67], off nt
	global_load_dwordx4 v[74:77], v[66:67], off offset:64 nt
	s_nop 0
	global_load_dwordx4 v[70:73], v[66:67], off offset:128 nt
	s_nop 0
	global_load_dwordx4 v[66:69], v[66:67], off offset:192 nt
	s_waitcnt vmcnt(0)
	v_mbcnt_lo_u32_b32 v221, -1, 0
	v_mbcnt_hi_u32_b32 v221, -1, v221
	v_and_b32_e32 v219, 7, v221
	v_lshrrev_b32_e32 v221, 4, v221
	v_lshlrev_b32_e32 v221, 5, v221
	v_and_b32_e32 v193, 1, v219
	v_lshrrev_b32_e32 v219, 1, v219
	v_lshlrev_b32_e32 v219, 7, v219
	v_lshl_or_b32 v219, v193, 4, v219
	v_readlane_b32 s0, v255, 18
	v_add_u32_e32 v221, v221, v219
	s_lshl_b32 s0, s0, 9
	s_add_i32 s0, s0, 0x12000
	v_add_u32_e32 v221, s0, v221
	ds_write_b128 v221, v[130:133]
	s_nop 1
	v_and_b32_e32 v221, 0xffff0000, v126
	v_and_b32_e32 v219, 0xffff0000, v127
	v_and_b32_e32 v193, 0xffff0000, v122
	v_and_b32_e32 v191, 0xffff0000, v123
	v_lshlrev_b32_e32 v223, 16, v126
	v_lshlrev_b32_e32 v220, 16, v127
	v_and_b32_e32 v213, 0xffff0000, v128
	v_lshlrev_b32_e32 v194, 16, v122
	v_lshlrev_b32_e32 v192, 16, v123
	v_and_b32_e32 v189, 0xffff0000, v124
	v_and_b32_e32 v179, 0xffff0000, v118
	v_and_b32_e32 v177, 0xffff0000, v119
	v_mul_f32_e32 v130, v221, v221
	v_mul_f32_e32 v131, v219, v219
	v_mul_f32_e32 v166, v193, v193
	v_mul_f32_e32 v167, v191, v191
	v_lshlrev_b32_e32 v214, 16, v128
	v_and_b32_e32 v211, 0xffff0000, v129
	v_lshlrev_b32_e32 v190, 16, v124
	v_and_b32_e32 v187, 0xffff0000, v125
	v_lshlrev_b32_e32 v180, 16, v118
	v_lshlrev_b32_e32 v178, 16, v119
	v_and_b32_e32 v175, 0xffff0000, v120
	v_mul_f32_e32 v132, v213, v213
	v_mul_f32_e32 v168, v189, v189
	v_mul_f32_e32 v170, v179, v179
	v_mul_f32_e32 v171, v177, v177
	v_fmac_f32_e32 v130, v223, v223
	v_fmac_f32_e32 v131, v220, v220
	v_fmac_f32_e32 v166, v194, v194
	v_fmac_f32_e32 v167, v192, v192
	v_lshlrev_b32_e32 v212, 16, v129
	v_lshlrev_b32_e32 v188, 16, v125
	v_lshlrev_b32_e32 v176, 16, v120
	v_and_b32_e32 v173, 0xffff0000, v121
	v_mul_f32_e32 v133, v211, v211
	v_mul_f32_e32 v169, v187, v187
	v_mul_f32_e32 v172, v175, v175
	v_fmac_f32_e32 v132, v214, v214
	v_fmac_f32_e32 v168, v190, v190
	v_fmac_f32_e32 v170, v180, v180
	v_fmac_f32_e32 v171, v178, v178
	v_add_f32_e32 v130, v130, v131
	v_add_f32_e32 v131, v166, v167
	v_lshlrev_b32_e32 v174, 16, v121
	v_mul_f32_e32 v181, v173, v173
	v_fmac_f32_e32 v133, v212, v212
	v_fmac_f32_e32 v169, v188, v188
	v_fmac_f32_e32 v172, v176, v176
	v_add_f32_e32 v166, v170, v171
	v_add_f32_e32 v130, v132, v130
	v_add_f32_e32 v131, v168, v131
	v_fmac_f32_e32 v181, v174, v174
	v_add_f32_e32 v132, v172, v166
	v_add_f32_e32 v130, v133, v130
	v_add_f32_e32 v131, v169, v131
	v_add_f32_e32 v132, v181, v132
	v_add_f32_e32 v130, v130, v131
	v_and_b32_e32 v172, 0xffff0000, v114
	v_and_b32_e32 v170, 0xffff0000, v115
	v_lshlrev_b32_e32 v165, 16, v114
	v_add_f32_e32 v130, v130, v132
	v_lshlrev_b32_e32 v171, 16, v115
	v_mul_f32_e32 v131, v172, v172
	v_mul_f32_e32 v132, v170, v170
	v_and_b32_e32 v168, 0xffff0000, v116
	v_fmac_f32_e32 v131, v165, v165
	v_fmac_f32_e32 v132, v171, v171
	v_lshlrev_b32_e32 v169, 16, v116
	v_add_f32_e32 v131, v131, v132
	v_mul_f32_e32 v132, v168, v168
	v_and_b32_e32 v166, 0xffff0000, v117
	v_fmac_f32_e32 v132, v169, v169
	v_lshlrev_b32_e32 v167, 16, v117
	v_add_f32_e32 v131, v132, v131
	v_mul_f32_e32 v132, v166, v166
	v_fmac_f32_e32 v132, v167, v167
	v_add_f32_e32 v131, v132, v131
	v_add_f32_e32 v130, v130, v131
	ds_bpermute_b32 v131, v156, v130
	s_waitcnt lgkmcnt(0)
	v_add_f32_e32 v181, v130, v131
	ds_bpermute_b32 v182, v157, v181
	s_and_saveexec_b64 s[0:1], s[4:5]
	s_cbranch_execz .LBB0_1039
	s_waitcnt lgkmcnt(0)
	v_add_f32_e32 v130, v181, v182
	ds_write_b32 v162, v130

.LBB0_1115:
	v_mbcnt_lo_u32_b32 v70, -1, 0
	v_mbcnt_hi_u32_b32 v70, -1, v70
	v_readlane_b32 s18, v255, 18
	v_lshrrev_b32_e32 v70, 4, v70
	s_lshl_b32 s18, s18, 9
	v_lshlrev_b32_e32 v70, 5, v70
	s_add_i32 s18, s18, 0x12000
	v_add_u32_e32 v70, s18, v70
	ds_read_b128 v[66:69], v70 offset:16
	ds_read_b128 v[70:73], v70
	ds_read_b32 v132, v153
	v_mov_b32_e32 v78, 0
	v_mov_b32_e32 v79, 0
	s_ashr_i32 s39, s38, 31
	s_lshl_b64 s[0:1], s[38:39], 16
	s_waitcnt lgkmcnt(0)
	v_mul_f32_e32 v74, v132, v223
	v_mul_f32_e32 v75, v132, v221
	v_mul_f32_e32 v76, v132, v220
	v_mul_f32_e32 v77, v132, v219
	s_waitcnt lgkmcnt(0)
	v_mul_f32_e32 v74, v70, v74
	v_mul_f32_e32 v75, v71, v75
	v_cvt_pk_fp8_f32 v78, v74, v75
	v_mul_f32_e32 v74, v132, v214
	v_mul_f32_e32 v75, v132, v213
	v_mul_f32_e32 v74, v66, v74
	v_mul_f32_e32 v75, v67, v75
	v_cvt_pk_fp8_f32 v79, v74, v75
	v_mul_f32_e32 v76, v72, v76
	v_mul_f32_e32 v77, v73, v77
	v_cvt_pk_fp8_f32 v78, v76, v77 op_sel:[0,0,1]
	v_mul_f32_e32 v76, v132, v212
	v_mul_f32_e32 v77, v132, v211
	v_mul_f32_e32 v76, v68, v76
	v_mul_f32_e32 v77, v69, v77
	v_cvt_pk_fp8_f32 v79, v76, v77 op_sel:[0,0,1]
	v_lshl_or_b32 v74, v252, 10, s0
	v_mov_b32_e32 v75, s1
	v_lshl_add_u64 v[76:77], v[140:141], 0, v[74:75]
	global_store_dwordx2 v[76:77], v[78:79], off
	ds_read2_b32 v[78:79], v153 offset1:16
	s_waitcnt lgkmcnt(0)
	v_mul_f32_e32 v82, v79, v229
	v_mul_f32_e32 v80, v79, v230
	v_mul_f32_e32 v81, v79, v228
	v_mul_f32_e32 v83, v72, v82
	v_mul_f32_e32 v82, v79, v227
	v_mul_f32_e32 v80, v70, v80
	v_mul_f32_e32 v81, v71, v81
	v_mul_f32_e32 v84, v73, v82
	v_mov_b32_e32 v82, 0
	v_cvt_pk_fp8_f32 v82, v80, v81
	v_mul_f32_e32 v80, v79, v217
	v_mul_f32_e32 v81, v79, v218
	v_mul_f32_e32 v80, v66, v80
	v_cvt_pk_fp8_f32 v82, v83, v84 op_sel:[0,0,1]
	v_mul_f32_e32 v83, v79, v216
	v_mul_f32_e32 v84, v68, v83
	v_mul_f32_e32 v83, v79, v215
	v_mul_f32_e32 v81, v67, v81
	v_mul_f32_e32 v85, v69, v83
	v_mov_b32_e32 v83, 0
	v_cvt_pk_fp8_f32 v83, v80, v81
	v_or_b32_e32 v80, 0x4000, v74
	v_mov_b32_e32 v81, s1
	v_cvt_pk_fp8_f32 v83, v84, v85 op_sel:[0,0,1]
	v_lshl_add_u64 v[84:85], v[140:141], 0, v[80:81]
	global_store_dwordx2 v[84:85], v[82:83], off
	ds_read2_b32 v[82:83], v153 offset0:16 offset1:32
	s_waitcnt lgkmcnt(0)
	v_mul_f32_e32 v86, v83, v233
	v_mul_f32_e32 v84, v83, v234
	v_mul_f32_e32 v85, v83, v232
	v_mul_f32_e32 v87, v72, v86
	v_mul_f32_e32 v86, v83, v231
	v_mul_f32_e32 v84, v70, v84
	v_mul_f32_e32 v85, v71, v85
	v_mul_f32_e32 v130, v73, v86
	v_mov_b32_e32 v86, 0
	v_cvt_pk_fp8_f32 v86, v84, v85
	v_mul_f32_e32 v84, v83, v225
	v_mul_f32_e32 v85, v83, v226
	v_mul_f32_e32 v84, v66, v84
	v_cvt_pk_fp8_f32 v86, v87, v130 op_sel:[0,0,1]
	v_mul_f32_e32 v87, v83, v224
	v_mul_f32_e32 v130, v68, v87
	v_mul_f32_e32 v87, v83, v222
	v_mul_f32_e32 v85, v67, v85
	v_mul_f32_e32 v131, v69, v87
	v_mov_b32_e32 v87, 0
	v_cvt_pk_fp8_f32 v87, v84, v85
	v_or_b32_e32 v84, 0x8000, v74
	v_mov_b32_e32 v85, s1
	v_or_b32_e32 v74, 0xc000, v74
	v_cvt_pk_fp8_f32 v87, v130, v131 op_sel:[0,0,1]
	v_lshl_add_u64 v[130:131], v[140:141], 0, v[84:85]
	global_store_dwordx2 v[130:131], v[86:87], off
	ds_read2_b32 v[86:87], v153 offset0:32 offset1:48
	s_waitcnt lgkmcnt(0)
	v_mul_f32_e32 v130, v87, v247
	v_mul_f32_e32 v130, v70, v130
	v_mul_f32_e32 v70, v87, v245
	v_mul_f32_e32 v71, v71, v70
	v_mul_f32_e32 v70, v87, v250
	v_mul_f32_e32 v72, v72, v70
	v_mul_f32_e32 v70, v87, v249
	v_mul_f32_e32 v73, v73, v70
	v_mov_b32_e32 v70, 0
	v_cvt_pk_fp8_f32 v70, v130, v71
	v_mul_f32_e32 v71, v87, v243
	v_mul_f32_e32 v66, v66, v71
	v_mul_f32_e32 v71, v87, v248
	v_mul_f32_e32 v67, v67, v71
	v_mul_f32_e32 v71, v87, v246
	v_mul_f32_e32 v68, v68, v71
	v_mul_f32_e32 v71, v87, v244
	v_mul_f32_e32 v69, v69, v71
	v_mov_b32_e32 v71, 0
	v_cvt_pk_fp8_f32 v71, v66, v67
	v_cvt_pk_fp8_f32 v70, v72, v73 op_sel:[0,0,1]
	v_lshl_add_u64 v[66:67], v[140:141], 0, v[74:75]
	v_mul_f32_e32 v130, v132, v194
	v_cvt_pk_fp8_f32 v71, v68, v69 op_sel:[0,0,1]
	global_store_dwordx2 v[66:67], v[70:71], off
	s_nop 1
	v_mbcnt_lo_u32_b32 v70, -1, 0
	v_mbcnt_hi_u32_b32 v70, -1, v70
	v_readlane_b32 s18, v255, 18
	v_lshrrev_b32_e32 v70, 4, v70
	s_lshl_b32 s18, s18, 9
	v_lshlrev_b32_e32 v70, 5, v70
	s_add_i32 s18, s18, 0x12080
	v_add_u32_e32 v70, s18, v70
	ds_read_b128 v[66:69], v70 offset:16
	ds_read_b128 v[70:73], v70
	s_waitcnt lgkmcnt(0)
	v_mul_f32_e32 v131, v70, v130
	v_mul_f32_e32 v130, v132, v193
	v_mul_f32_e32 v133, v71, v130
	v_mul_f32_e32 v130, v132, v192
	v_mul_f32_e32 v192, v72, v130
	v_mul_f32_e32 v130, v132, v191
	v_mul_f32_e32 v191, v73, v130
	v_mov_b32_e32 v130, 0
	v_cvt_pk_fp8_f32 v130, v131, v133
	v_mul_f32_e32 v131, v132, v190
	v_mul_f32_e32 v133, v66, v131
	v_mul_f32_e32 v131, v132, v189
	v_mul_f32_e32 v189, v67, v131
	v_mul_f32_e32 v131, v132, v188
	v_mul_f32_e32 v188, v68, v131
	v_mul_f32_e32 v131, v132, v187
	v_mul_f32_e32 v132, v69, v131
	v_mov_b32_e32 v131, 0
	v_cvt_pk_fp8_f32 v131, v133, v189
	v_cvt_pk_fp8_f32 v130, v192, v191 op_sel:[0,0,1]
	v_cvt_pk_fp8_f32 v131, v188, v132 op_sel:[0,0,1]
	global_store_dwordx2 v[76:77], v[130:131], off offset:32
	v_mul_f32_e32 v130, v79, v201
	v_mul_f32_e32 v131, v70, v130
	v_mul_f32_e32 v130, v79, v202
	v_mul_f32_e32 v132, v71, v130
	v_mul_f32_e32 v130, v79, v200
	v_mul_f32_e32 v133, v72, v130
	v_mul_f32_e32 v130, v79, v199
	v_mul_f32_e32 v187, v73, v130
	v_mov_b32_e32 v130, 0
	v_cvt_pk_fp8_f32 v130, v131, v132
	v_mul_f32_e32 v131, v79, v198
	v_mul_f32_e32 v132, v66, v131
	v_mul_f32_e32 v131, v79, v197
	v_cvt_pk_fp8_f32 v130, v133, v187 op_sel:[0,0,1]
	v_mul_f32_e32 v133, v67, v131
	v_mul_f32_e32 v131, v79, v195
	v_mul_f32_e32 v187, v68, v131
	v_mov_b32_e32 v131, 0
	v_cvt_pk_fp8_f32 v131, v132, v133
	v_mul_f32_e32 v79, v79, v196
	v_mul_f32_e32 v79, v69, v79
	v_lshl_add_u64 v[132:133], v[144:145], 0, v[80:81]
	v_cvt_pk_fp8_f32 v131, v187, v79 op_sel:[0,0,1]
	v_mul_f32_e32 v79, v83, v209
	v_mul_f32_e32 v79, v70, v79
	global_store_dwordx2 v[132:133], v[130:131], off
	v_mul_f32_e32 v130, v83, v210
	v_mul_f32_e32 v131, v71, v130
	v_mul_f32_e32 v130, v83, v208
	v_mul_f32_e32 v132, v72, v130
	v_mul_f32_e32 v130, v83, v207
	v_mul_f32_e32 v133, v73, v130
	v_mov_b32_e32 v130, 0
	v_cvt_pk_fp8_f32 v130, v79, v131
	v_mul_f32_e32 v131, v83, v205
	v_mul_f32_e32 v79, v83, v206
	v_mul_f32_e32 v79, v66, v79
	v_cvt_pk_fp8_f32 v130, v132, v133 op_sel:[0,0,1]
	v_mul_f32_e32 v132, v67, v131
	v_mul_f32_e32 v131, v83, v203
	v_mul_f32_e32 v133, v68, v131
	v_mov_b32_e32 v131, 0
	v_cvt_pk_fp8_f32 v131, v79, v132
	v_mul_f32_e32 v79, v87, v236
	v_mul_f32_e32 v79, v70, v79
	v_mul_f32_e32 v70, v87, v242
	v_mul_f32_e32 v71, v71, v70
	v_mul_f32_e32 v70, v87, v240
	v_mul_f32_e32 v72, v72, v70
	v_mul_f32_e32 v70, v87, v238
	v_mul_f32_e32 v73, v73, v70
	v_mov_b32_e32 v70, 0
	v_cvt_pk_fp8_f32 v70, v79, v71
	v_mul_f32_e32 v71, v87, v239
	v_mul_f32_e32 v66, v66, v71
	v_mul_f32_e32 v71, v87, v237
	v_mul_f32_e32 v67, v67, v71
	v_mul_f32_e32 v71, v87, v235
	v_mul_f32_e32 v83, v83, v204
	v_mul_f32_e32 v68, v68, v71
	v_mul_f32_e32 v71, v87, v241
	v_mul_f32_e32 v83, v69, v83
	v_mul_f32_e32 v69, v69, v71
	v_mov_b32_e32 v71, 0
	v_cvt_pk_fp8_f32 v71, v66, v67
	v_cvt_pk_fp8_f32 v131, v133, v83 op_sel:[0,0,1]
	v_cvt_pk_fp8_f32 v70, v72, v73 op_sel:[0,0,1]
	v_lshl_add_u64 v[132:133], v[144:145], 0, v[84:85]
	v_cvt_pk_fp8_f32 v71, v68, v69 op_sel:[0,0,1]
	v_lshl_add_u64 v[66:67], v[144:145], 0, v[74:75]
	global_store_dwordx2 v[132:133], v[130:131], off
	global_store_dwordx2 v[66:67], v[70:71], off
	s_nop 1
	v_mbcnt_lo_u32_b32 v70, -1, 0
	v_mbcnt_hi_u32_b32 v70, -1, v70
	v_readlane_b32 s18, v255, 18
	v_lshrrev_b32_e32 v70, 4, v70
	s_lshl_b32 s18, s18, 9
	v_lshlrev_b32_e32 v70, 5, v70
	s_add_i32 s18, s18, 0x12100
	v_add_u32_e32 v70, s18, v70
	ds_read_b128 v[66:69], v70 offset:16
	ds_read_b128 v[70:73], v70
	ds_read_b32 v79, v153
	s_waitcnt lgkmcnt(0)
	v_mul_f32_e32 v130, v79, v178
	v_mul_f32_e32 v83, v79, v180
	v_mul_f32_e32 v87, v79, v179
	s_waitcnt lgkmcnt(0)
	v_mul_f32_e32 v131, v72, v130
	v_mul_f32_e32 v130, v79, v177
	v_mul_f32_e32 v83, v70, v83
	v_mul_f32_e32 v87, v71, v87
	v_mul_f32_e32 v132, v73, v130
	v_mov_b32_e32 v130, 0
	v_cvt_pk_fp8_f32 v130, v83, v87
	v_mul_f32_e32 v83, v79, v176
	v_mul_f32_e32 v87, v79, v175
	v_mul_f32_e32 v83, v66, v83
	v_cvt_pk_fp8_f32 v130, v131, v132 op_sel:[0,0,1]
	v_mul_f32_e32 v131, v79, v174
	v_mul_f32_e32 v87, v67, v87
	v_mul_f32_e32 v132, v68, v131
	v_mov_b32_e32 v131, 0
	v_cvt_pk_fp8_f32 v131, v83, v87
	v_mul_f32_e32 v79, v79, v173
	v_mul_f32_e32 v79, v69, v79
	v_cvt_pk_fp8_f32 v131, v132, v79 op_sel:[0,0,1]
	ds_read_b32 v79, v153 offset:64
	global_store_dwordx2 v[76:77], v[130:131], off offset:64
	s_waitcnt lgkmcnt(0)
	v_mul_f32_e32 v130, v79, v183
	v_mul_f32_e32 v83, v79, v184
	v_mul_f32_e32 v87, v79, v182
	v_mul_f32_e32 v131, v72, v130
	v_mul_f32_e32 v130, v79, v181
	v_mul_f32_e32 v83, v70, v83
	v_mul_f32_e32 v87, v71, v87
	v_mul_f32_e32 v132, v73, v130
	v_mov_b32_e32 v130, 0
	v_cvt_pk_fp8_f32 v130, v83, v87
	v_mul_f32_e32 v83, v79, v128
	v_mul_f32_e32 v87, v79, v129
	v_mul_f32_e32 v83, v66, v83
	v_cvt_pk_fp8_f32 v130, v131, v132 op_sel:[0,0,1]
	v_mul_f32_e32 v87, v67, v87
	v_mov_b32_e32 v131, 0
	v_cvt_pk_fp8_f32 v131, v83, v87
	v_mul_f32_e32 v127, v79, v127
	v_mul_f32_e32 v79, v79, v126
	v_mul_f32_e32 v127, v68, v127
	v_mul_f32_e32 v79, v69, v79
	v_cvt_pk_fp8_f32 v131, v127, v79 op_sel:[0,0,1]
	ds_read_b32 v79, v153 offset:128
	v_lshl_add_u64 v[126:127], v[146:147], 0, v[80:81]
	global_store_dwordx2 v[126:127], v[130:131], off
	s_waitcnt lgkmcnt(0)
	v_mul_f32_e32 v83, v79, v117
	v_mul_f32_e32 v87, v79, v115
	v_mul_f32_e32 v114, v79, v114
	v_mul_f32_e32 v83, v70, v83
	v_mul_f32_e32 v87, v71, v87
	v_mul_f32_e32 v115, v79, v116
	v_mul_f32_e32 v116, v73, v114
	v_mov_b32_e32 v114, 0
	v_cvt_pk_fp8_f32 v114, v83, v87
	v_mul_f32_e32 v115, v72, v115
	v_mul_f32_e32 v83, v79, v112
	v_mul_f32_e32 v87, v79, v113
	v_cvt_pk_fp8_f32 v114, v115, v116 op_sel:[0,0,1]
	v_mul_f32_e32 v83, v66, v83
	v_mul_f32_e32 v87, v67, v87
	v_mov_b32_e32 v115, 0
	v_cvt_pk_fp8_f32 v115, v83, v87
	v_mul_f32_e32 v111, v79, v111
	v_mul_f32_e32 v79, v79, v110
	v_mul_f32_e32 v111, v68, v111
	v_mul_f32_e32 v79, v69, v79
	v_cvt_pk_fp8_f32 v115, v111, v79 op_sel:[0,0,1]
	ds_read_b32 v79, v153 offset:192
	v_lshl_add_u64 v[110:111], v[146:147], 0, v[84:85]
	v_mul_f32_e32 v87, v78, v171
	global_store_dwordx2 v[110:111], v[114:115], off
	s_waitcnt lgkmcnt(0)
	v_mul_f32_e32 v83, v79, v100
	v_mul_f32_e32 v83, v70, v83
	v_mul_f32_e32 v70, v79, v98
	v_mul_f32_e32 v71, v71, v70
	v_mul_f32_e32 v70, v79, v186
	v_mul_f32_e32 v72, v72, v70
	v_mul_f32_e32 v70, v79, v185
	v_mul_f32_e32 v73, v73, v70
	v_mov_b32_e32 v70, 0
	v_cvt_pk_fp8_f32 v70, v83, v71
	v_mul_f32_e32 v71, v79, v96
	v_mul_f32_e32 v66, v66, v71
	v_mul_f32_e32 v71, v79, v101
	v_mul_f32_e32 v67, v67, v71
	v_mul_f32_e32 v71, v79, v99
	v_mul_f32_e32 v68, v68, v71
	v_mul_f32_e32 v71, v79, v97
	v_mul_f32_e32 v69, v69, v71
	v_mov_b32_e32 v71, 0
	v_cvt_pk_fp8_f32 v71, v66, v67
	v_cvt_pk_fp8_f32 v70, v72, v73 op_sel:[0,0,1]
	v_lshl_add_u64 v[66:67], v[146:147], 0, v[74:75]
	v_mul_f32_e32 v79, v78, v165
	v_cvt_pk_fp8_f32 v71, v68, v69 op_sel:[0,0,1]
	v_mul_f32_e32 v83, v78, v172
	v_mul_f32_e32 v96, v78, v170
	global_store_dwordx2 v[66:67], v[70:71], off
	s_nop 1
	v_mbcnt_lo_u32_b32 v70, -1, 0
	v_mbcnt_hi_u32_b32 v70, -1, v70
	v_readlane_b32 s18, v255, 18
	v_lshrrev_b32_e32 v70, 4, v70
	s_lshl_b32 s18, s18, 9
	v_lshlrev_b32_e32 v70, 5, v70
	s_add_i32 s18, s18, 0x12180
	v_add_u32_e32 v70, s18, v70
	ds_read_b128 v[66:69], v70 offset:16
	ds_read_b128 v[70:73], v70
	s_waitcnt lgkmcnt(0)
	v_mul_f32_e32 v79, v70, v79
	v_mul_f32_e32 v83, v71, v83
	v_mul_f32_e32 v97, v73, v96
	v_mov_b32_e32 v96, 0
	v_cvt_pk_fp8_f32 v96, v79, v83
	v_mul_f32_e32 v87, v72, v87
	v_mul_f32_e32 v79, v78, v169
	v_mul_f32_e32 v83, v78, v168
	v_cvt_pk_fp8_f32 v96, v87, v97 op_sel:[0,0,1]
	v_mul_f32_e32 v79, v66, v79
	v_mul_f32_e32 v83, v67, v83
	v_mov_b32_e32 v97, 0
	v_cvt_pk_fp8_f32 v97, v79, v83
	v_mul_f32_e32 v87, v78, v167
	v_mul_f32_e32 v78, v78, v166
	v_mul_f32_e32 v87, v68, v87
	v_mul_f32_e32 v78, v69, v78
	v_cvt_pk_fp8_f32 v97, v87, v78 op_sel:[0,0,1]
	global_store_dwordx2 v[76:77], v[96:97], off offset:96
	v_mul_f32_e32 v76, v82, v125
	v_mul_f32_e32 v77, v70, v76
	v_mul_f32_e32 v76, v82, v124
	v_mul_f32_e32 v78, v71, v76
	v_mul_f32_e32 v76, v82, v123
	v_mul_f32_e32 v79, v72, v76
	v_mul_f32_e32 v76, v82, v122
	v_mul_f32_e32 v83, v73, v76
	v_mov_b32_e32 v76, 0
	v_cvt_pk_fp8_f32 v76, v77, v78
	v_mul_f32_e32 v77, v82, v121
	v_mul_f32_e32 v78, v66, v77
	v_mul_f32_e32 v77, v82, v120
	v_cvt_pk_fp8_f32 v76, v79, v83 op_sel:[0,0,1]
	v_mul_f32_e32 v79, v67, v77
	v_mul_f32_e32 v77, v82, v119
	v_mul_f32_e32 v83, v68, v77
	v_mul_f32_e32 v77, v82, v118
	v_mul_f32_e32 v82, v69, v77
	v_mov_b32_e32 v77, 0
	v_cvt_pk_fp8_f32 v77, v78, v79
	v_lshl_add_u64 v[78:79], v[148:149], 0, v[80:81]
	v_cvt_pk_fp8_f32 v77, v83, v82 op_sel:[0,0,1]
	global_store_dwordx2 v[78:79], v[76:77], off
	v_mul_f32_e32 v76, v86, v109
	v_mul_f32_e32 v77, v70, v76
	v_mul_f32_e32 v76, v86, v108
	v_mul_f32_e32 v78, v71, v76
	v_mul_f32_e32 v76, v86, v107
	v_mul_f32_e32 v79, v72, v76
	v_mul_f32_e32 v76, v86, v106
	v_mul_f32_e32 v80, v73, v76
	v_mov_b32_e32 v76, 0
	v_cvt_pk_fp8_f32 v76, v77, v78
	v_mul_f32_e32 v77, v86, v105
	v_mul_f32_e32 v78, v66, v77
	v_mul_f32_e32 v77, v86, v104
	v_cvt_pk_fp8_f32 v76, v79, v80 op_sel:[0,0,1]
	v_mul_f32_e32 v79, v67, v77
	v_mul_f32_e32 v77, v86, v103
	v_mul_f32_e32 v80, v68, v77
	v_mul_f32_e32 v77, v86, v102
	v_mul_f32_e32 v81, v69, v77
	v_mov_b32_e32 v77, 0
	v_cvt_pk_fp8_f32 v77, v78, v79
	v_lshl_add_u64 v[78:79], v[148:149], 0, v[84:85]
	v_cvt_pk_fp8_f32 v77, v80, v81 op_sel:[0,0,1]
	global_store_dwordx2 v[78:79], v[76:77], off
	ds_read_b32 v76, v153 offset:192
	s_waitcnt lgkmcnt(0)
	v_mul_f32_e32 v77, v76, v95
	v_mul_f32_e32 v77, v70, v77
	v_mul_f32_e32 v70, v76, v94
	v_mul_f32_e32 v71, v71, v70
	v_mul_f32_e32 v70, v76, v93
	v_mul_f32_e32 v72, v72, v70
	v_mul_f32_e32 v70, v76, v92
	v_mul_f32_e32 v73, v73, v70
	v_mov_b32_e32 v70, 0
	v_cvt_pk_fp8_f32 v70, v77, v71
	v_mul_f32_e32 v71, v76, v91
	v_mul_f32_e32 v66, v66, v71
	v_mul_f32_e32 v71, v76, v90
	v_mul_f32_e32 v67, v67, v71
	v_mul_f32_e32 v71, v76, v89
	v_mul_f32_e32 v68, v68, v71
	v_mul_f32_e32 v71, v76, v88
	v_mul_f32_e32 v69, v69, v71
	v_mov_b32_e32 v71, 0
	v_cvt_pk_fp8_f32 v71, v66, v67
	v_cvt_pk_fp8_f32 v70, v72, v73 op_sel:[0,0,1]
	v_lshl_add_u64 v[66:67], v[148:149], 0, v[74:75]
	v_cvt_pk_fp8_f32 v71, v68, v69 op_sel:[0,0,1]
	global_store_dwordx2 v[66:67], v[70:71], off
	s_barrier
	s_and_saveexec_b64 s[0:1], s[22:23]
	s_cbranch_execz .LBB0_1117
	ds_read_b32 v66, v253
	s_waitcnt lgkmcnt(0)
	global_atomic_add v66, v[142:143], v66, off sc0
	s_waitcnt vmcnt(0)
	ds_write_b32 v254, v66
